# speedup vs baseline: 1.0065x; 1.0050x over previous
.Lm_norescale0:
	s_waitcnt lgkmcnt(3)
	v_mfma_f32_32x32x16_f16 v[74:89], v[154:157], v[70:73], v[74:89]
	ds_read_b128 v[154:157], v218 offset:1024
	v_exp_f32_e32 v234, v126
	v_exp_f32_e32 v235, v127
	v_exp_f32_e32 v236, v128
	v_exp_f32_e32 v237, v129
	v_exp_f32_e32 v238, v130
	v_exp_f32_e32 v239, v131
	v_exp_f32_e32 v240, v132
	v_exp_f32_e32 v241, v133
	s_waitcnt lgkmcnt(3)
	v_mfma_f32_32x32x16_f16 v[74:89], v[242:245], v[90:93], v[74:89]
	v_exp_f32_e32 v106, v134
	v_exp_f32_e32 v107, v135
	v_exp_f32_e32 v108, v136
	v_exp_f32_e32 v109, v137
	v_exp_f32_e32 v110, v138
	v_exp_f32_e32 v111, v139
	v_exp_f32_e32 v112, v140
	v_exp_f32_e32 v113, v141
	v_pk_add_f32 v[50:51], v[234:235], v[50:51]
	v_pk_add_f32 v[52:53], v[236:237], v[52:53]
	v_pk_add_f32 v[54:55], v[238:239], v[54:55]
	v_pk_add_f32 v[56:57], v[240:241], v[56:57]
	s_waitcnt lgkmcnt(2)
	v_mfma_f32_32x32x16_f16 v[74:89], v[246:249], v[94:97], v[74:89]
	v_pk_add_f32 v[58:59], v[106:107], v[58:59]
	v_pk_add_f32 v[60:61], v[108:109], v[60:61]
	v_pk_add_f32 v[62:63], v[110:111], v[62:63]
	v_pk_add_f32 v[64:65], v[112:113], v[64:65]
	v_fma_mix_f32 v216, v234, v114, v216 op_sel:[0,0,0] op_sel_hi:[0,1,0]
	v_fma_mix_f32 v217, v235, v114, v217 op_sel:[0,1,0] op_sel_hi:[0,1,0]
	v_fma_mix_f32 v214, v236, v115, v214 op_sel:[0,0,0] op_sel_hi:[0,1,0]
	v_fma_mix_f32 v215, v237, v115, v215 op_sel:[0,1,0] op_sel_hi:[0,1,0]
	v_fma_mix_f32 v212, v238, v116, v212 op_sel:[0,0,0] op_sel_hi:[0,1,0]
	v_fma_mix_f32 v213, v239, v116, v213 op_sel:[0,1,0] op_sel_hi:[0,1,0]
	v_fma_mix_f32 v210, v240, v117, v210 op_sel:[0,0,0] op_sel_hi:[0,1,0]
	v_fma_mix_f32 v211, v241, v117, v211 op_sel:[0,1,0] op_sel_hi:[0,1,0]
	v_fma_mix_f32 v208, v106, v118, v208 op_sel:[0,0,0] op_sel_hi:[0,1,0]
	v_fma_mix_f32 v209, v107, v118, v209 op_sel:[0,1,0] op_sel_hi:[0,1,0]
	v_fma_mix_f32 v204, v108, v119, v204 op_sel:[0,0,0] op_sel_hi:[0,1,0]
	v_fma_mix_f32 v205, v109, v119, v205 op_sel:[0,1,0] op_sel_hi:[0,1,0]
	v_fma_mix_f32 v202, v110, v120, v202 op_sel:[0,0,0] op_sel_hi:[0,1,0]
	v_fma_mix_f32 v203, v111, v120, v203 op_sel:[0,1,0] op_sel_hi:[0,1,0]
	v_fma_mix_f32 v196, v112, v121, v196 op_sel:[0,0,0] op_sel_hi:[0,1,0]
	v_fma_mix_f32 v197, v113, v121, v197 op_sel:[0,1,0] op_sel_hi:[0,1,0]
	s_setprio 1
	v_max3_f32 v254, v74, v75, v76
	v_max3_f32 v255, v77, v78, v79
	v_max3_f32 v254, v254, v80, v81
	v_max3_f32 v255, v255, v82, v83
	v_max3_f32 v254, v254, v84, v85
	v_max3_f32 v255, v255, v86, v87
	v_max3_f32 v254, v254, v88, v89
	v_max_f32_e32 v254, v254, v255
	v_cmp_lt_f32_e32 vcc, s5, v254
	s_cbranch_vccz .Lm_norescale1
	v_max_f32_e32 v234, 0, v74
	v_max_f32_e32 v235, 0, v75
	v_max_f32_e32 v236, 0, v76
	v_max_f32_e32 v237, 0, v77
	v_max_f32_e32 v238, 0, v78
	v_max_f32_e32 v239, 0, v79
	v_max_f32_e32 v240, 0, v80
	v_max_f32_e32 v241, 0, v81
	v_max_f32_e32 v106, 0, v82
	v_max_f32_e32 v107, 0, v83
	v_max_f32_e32 v108, 0, v84
	v_max_f32_e32 v109, 0, v85
	v_max_f32_e32 v110, 0, v86
	v_max_f32_e32 v111, 0, v87
	v_max_f32_e32 v112, 0, v88
	v_max_f32_e32 v113, 0, v89
	v_sub_f32_e32 v74, v74, v234
	v_sub_f32_e32 v75, v75, v235
	v_sub_f32_e32 v76, v76, v236
	v_sub_f32_e32 v77, v77, v237
	v_sub_f32_e32 v78, v78, v238
	v_sub_f32_e32 v79, v79, v239
	v_sub_f32_e32 v80, v80, v240
	v_sub_f32_e32 v81, v81, v241
	v_sub_f32_e32 v82, v82, v106
	v_sub_f32_e32 v83, v83, v107
	v_sub_f32_e32 v84, v84, v108
	v_sub_f32_e32 v85, v85, v109
	v_sub_f32_e32 v86, v86, v110
	v_sub_f32_e32 v87, v87, v111
	v_sub_f32_e32 v88, v88, v112
	v_sub_f32_e32 v89, v89, v113
	v_sub_f32_e32 v34, v34, v234
	v_sub_f32_e32 v35, v35, v235
	v_sub_f32_e32 v36, v36, v236
	v_sub_f32_e32 v37, v37, v237
	v_sub_f32_e32 v38, v38, v238
	v_sub_f32_e32 v39, v39, v239
	v_sub_f32_e32 v40, v40, v240
	v_sub_f32_e32 v41, v41, v241
	v_sub_f32_e32 v42, v42, v106
	v_sub_f32_e32 v43, v43, v107
	v_sub_f32_e32 v44, v44, v108
	v_sub_f32_e32 v45, v45, v109
	v_sub_f32_e32 v46, v46, v110
	v_sub_f32_e32 v47, v47, v111
	v_sub_f32_e32 v48, v48, v112
	v_sub_f32_e32 v49, v49, v113
	v_exp_f32_e64 v234, -v234
	v_exp_f32_e64 v235, -v235
	v_exp_f32_e64 v236, -v236
	v_exp_f32_e64 v237, -v237
	v_exp_f32_e64 v238, -v238
	v_exp_f32_e64 v239, -v239
	v_exp_f32_e64 v240, -v240
	v_exp_f32_e64 v241, -v241
	v_exp_f32_e64 v106, -v106
	v_exp_f32_e64 v107, -v107
	v_exp_f32_e64 v108, -v108
	v_exp_f32_e64 v109, -v109
	v_exp_f32_e64 v110, -v110
	v_exp_f32_e64 v111, -v111
	v_exp_f32_e64 v112, -v112
	v_exp_f32_e64 v113, -v113
	s_nop 0
	v_mul_f32_e32 v18, v234, v18
	v_mul_f32_e32 v19, v235, v19
	v_mul_f32_e32 v20, v236, v20
	v_mul_f32_e32 v21, v237, v21
	v_mul_f32_e32 v22, v238, v22
	v_mul_f32_e32 v23, v239, v23
	v_mul_f32_e32 v24, v240, v24
	v_mul_f32_e32 v25, v241, v25
	v_mul_f32_e32 v26, v106, v26
	v_mul_f32_e32 v27, v107, v27
	v_mul_f32_e32 v28, v108, v28
	v_mul_f32_e32 v29, v109, v29
	v_mul_f32_e32 v30, v110, v30
	v_mul_f32_e32 v31, v111, v31
	v_mul_f32_e32 v32, v112, v32
	v_mul_f32_e32 v33, v113, v33
	v_mul_f32_e32 v206, v234, v206
	v_mul_f32_e32 v207, v235, v207
	v_mul_f32_e32 v200, v236, v200
	v_mul_f32_e32 v201, v237, v201
	v_mul_f32_e32 v198, v238, v198
	v_mul_f32_e32 v199, v239, v199
	v_mul_f32_e32 v194, v240, v194
	v_mul_f32_e32 v195, v241, v195
	v_mul_f32_e32 v192, v106, v192
	v_mul_f32_e32 v193, v107, v193
	v_mul_f32_e32 v190, v108, v190
	v_mul_f32_e32 v191, v109, v191
	v_mul_f32_e32 v188, v110, v188
	v_mul_f32_e32 v189, v111, v189
	v_mul_f32_e32 v186, v112, v186
	v_mul_f32_e32 v187, v113, v187
	s_nop 1
